# plan E conversion partition + LRU counted vmcnt + out-proj-0 epilogue base loads issued in bursts
# baseline (speedup 1.0000x reference)
.LBB0_502:
	s_lshl_b32 s44, s77, 8
	v_lshrrev_b32_e32 v40, 1, v44
	s_add_i32 s44, s44, s67
	v_and_b32_e32 v40, 24, v40
	v_lshl_or_b32 v40, s76, 8, v40
	v_and_or_b32 v152, v44, 15, s44
	v_or_b32_e32 v56, s68, v40
	s_lshl_b64 s[42:43], s[42:43], 2
	v_ashrrev_i32_e32 v153, 31, v152
	s_add_u32 s42, s6, s42
	v_ashrrev_i32_e32 v57, 31, v56
	v_lshlrev_b64 v[44:45], 12, v[152:153]
	s_addc_u32 s43, s7, s43
	v_lshlrev_b64 v[148:149], 2, v[56:57]
	v_lshl_add_u64 v[154:155], s[10:11], 0, v[44:45]
	v_lshl_add_u64 v[46:47], s[42:43], 0, v[148:149]
	v_lshl_add_u64 v[58:59], s[8:9], 0, v[44:45]
	v_lshl_add_u64 v[44:45], v[154:155], 0, s[20:21]
	v_add_co_u32_e32 v40, vcc, s74, v46
	v_cndmask_b32_e64 v45, v45, v59, s[2:3]
	v_cndmask_b32_e64 v44, v44, v58, s[2:3]
	v_addc_co_u32_e32 v41, vcc, 0, v47, vcc
	v_lshl_add_u64 v[174:175], v[44:45], 0, v[148:149]
	global_load_dwordx4 v[40:43], v[40:41], off
	s_nop 0
	s_nop 0
	s_nop 0
	v_lshl_add_u64 v[58:59], v[46:47], 0, s[18:19]
	global_load_dwordx4 v[44:47], v[58:59], off offset:16
	v_lshlrev_b64 v[60:61], 11, v[152:153]
	v_lshl_add_u64 v[60:61], s[14:15], 0, v[60:61]
	v_lshlrev_b64 v[150:151], 1, v[56:57]
	v_lshl_add_u64 v[176:177], v[60:61], 0, v[150:151]
	global_load_dwordx4 v[60:63], v[58:59], off offset:512
	s_nop 0
	global_load_dwordx4 v[56:59], v[58:59], off offset:528
	s_andn2_b64 vcc, exec, s[0:1]
	s_mov_b64 s[0:1], -1
	s_mov_b64 s[90:91], 0x10000
	s_mov_b64 s[92:93], 0x50000
	s_mov_b64 s[96:97], 0x8000
	global_load_dwordx4 v[178:181], v[174:175], off
	global_load_dwordx4 v[182:185], v[174:175], off offset:16
	global_load_dwordx4 v[186:189], v[174:175], off offset:512
	global_load_dwordx4 v[190:193], v[174:175], off offset:528
	v_lshl_add_u64 v[234:235], v[174:175], 0, s[90:91]
	global_load_dwordx4 v[194:197], v[234:235], off
	global_load_dwordx4 v[198:201], v[234:235], off offset:16
	global_load_dwordx4 v[202:205], v[234:235], off offset:512
	global_load_dwordx4 v[206:209], v[234:235], off offset:528
	v_lshl_add_u64 v[234:235], v[234:235], 0, s[90:91]
	global_load_dwordx4 v[210:213], v[234:235], off
	global_load_dwordx4 v[214:217], v[234:235], off offset:16
	global_load_dwordx4 v[218:221], v[234:235], off offset:512
	global_load_dwordx4 v[222:225], v[234:235], off offset:528
	v_lshl_add_u64 v[234:235], v[234:235], 0, s[90:91]
	global_load_dwordx4 v[226:229], v[234:235], off
	global_load_dwordx4 v[230:233], v[234:235], off offset:16
	global_load_dwordx4 v[244:247], v[234:235], off offset:512
	global_load_dwordx4 v[248:251], v[234:235], off offset:528
	s_waitcnt vmcnt(14)
	v_pk_fma_f32 v[138:139], v[138:139], v[42:43], v[180:181]
	v_pk_fma_f32 v[136:137], v[136:137], v[40:41], v[178:179]
	v_pk_fma_f32 v[142:143], v[142:143], v[46:47], v[184:185]
	v_pk_fma_f32 v[140:141], v[140:141], v[44:45], v[182:183]
	v_cvt_pk_bf16_f32 v136, v136, v137
	v_cvt_pk_bf16_f32 v137, v138, v139
	v_cvt_pk_bf16_f32 v138, v140, v141
	v_cvt_pk_bf16_f32 v139, v142, v143
	global_store_dwordx4 v[176:177], v[136:139], off
	v_lshl_add_u64 v[234:235], v[234:235], 0, s[92:93]
	global_load_dwordx4 v[178:181], v[234:235], off
	global_load_dwordx4 v[182:185], v[234:235], off offset:16
	s_waitcnt vmcnt(15)
	v_pk_fma_f32 v[130:131], v[130:131], v[62:63], v[188:189]
	v_pk_fma_f32 v[128:129], v[128:129], v[60:61], v[186:187]
	v_pk_fma_f32 v[134:135], v[134:135], v[58:59], v[192:193]
	v_pk_fma_f32 v[132:133], v[132:133], v[56:57], v[190:191]
	v_cvt_pk_bf16_f32 v128, v128, v129
	v_cvt_pk_bf16_f32 v129, v130, v131
	v_cvt_pk_bf16_f32 v130, v132, v133
	v_cvt_pk_bf16_f32 v131, v134, v135
	global_store_dwordx4 v[176:177], v[128:131], off offset:256
	global_load_dwordx4 v[186:189], v[234:235], off offset:512
	global_load_dwordx4 v[190:193], v[234:235], off offset:528
	s_waitcnt vmcnt(16)
	v_pk_fma_f32 v[122:123], v[122:123], v[42:43], v[196:197]
	v_pk_fma_f32 v[120:121], v[120:121], v[40:41], v[194:195]
	v_pk_fma_f32 v[126:127], v[126:127], v[46:47], v[200:201]
	v_pk_fma_f32 v[124:125], v[124:125], v[44:45], v[198:199]
	v_cvt_pk_bf16_f32 v120, v120, v121
	v_cvt_pk_bf16_f32 v121, v122, v123
	v_cvt_pk_bf16_f32 v122, v124, v125
	v_cvt_pk_bf16_f32 v123, v126, v127
	v_lshl_add_u64 v[236:237], v[176:177], 0, s[96:97]
	global_store_dwordx4 v[236:237], v[120:123], off
	v_lshl_add_u64 v[234:235], v[234:235], 0, s[90:91]
	global_load_dwordx4 v[194:197], v[234:235], off
	global_load_dwordx4 v[198:201], v[234:235], off offset:16
	s_waitcnt vmcnt(17)
	v_pk_fma_f32 v[114:115], v[114:115], v[62:63], v[204:205]
	v_pk_fma_f32 v[112:113], v[112:113], v[60:61], v[202:203]
	v_pk_fma_f32 v[118:119], v[118:119], v[58:59], v[208:209]
	v_pk_fma_f32 v[116:117], v[116:117], v[56:57], v[206:207]
	v_cvt_pk_bf16_f32 v112, v112, v113
	v_cvt_pk_bf16_f32 v113, v114, v115
	v_cvt_pk_bf16_f32 v114, v116, v117
	v_cvt_pk_bf16_f32 v115, v118, v119
	global_store_dwordx4 v[236:237], v[112:115], off offset:256
	global_load_dwordx4 v[202:205], v[234:235], off offset:512
	global_load_dwordx4 v[206:209], v[234:235], off offset:528
	s_waitcnt vmcnt(18)
	v_pk_fma_f32 v[106:107], v[106:107], v[42:43], v[212:213]
	v_pk_fma_f32 v[104:105], v[104:105], v[40:41], v[210:211]
	v_pk_fma_f32 v[110:111], v[110:111], v[46:47], v[216:217]
	v_pk_fma_f32 v[108:109], v[108:109], v[44:45], v[214:215]
	v_cvt_pk_bf16_f32 v104, v104, v105
	v_cvt_pk_bf16_f32 v105, v106, v107
	v_cvt_pk_bf16_f32 v106, v108, v109
	v_cvt_pk_bf16_f32 v107, v110, v111
	v_lshl_add_u64 v[236:237], v[236:237], 0, s[96:97]
	global_store_dwordx4 v[236:237], v[104:107], off
	v_lshl_add_u64 v[234:235], v[234:235], 0, s[90:91]
	global_load_dwordx4 v[210:213], v[234:235], off
	global_load_dwordx4 v[214:217], v[234:235], off offset:16
	s_waitcnt vmcnt(19)
	v_pk_fma_f32 v[98:99], v[98:99], v[62:63], v[220:221]
	v_pk_fma_f32 v[96:97], v[96:97], v[60:61], v[218:219]
	v_pk_fma_f32 v[102:103], v[102:103], v[58:59], v[224:225]
	v_pk_fma_f32 v[100:101], v[100:101], v[56:57], v[222:223]
	v_cvt_pk_bf16_f32 v96, v96, v97
	v_cvt_pk_bf16_f32 v97, v98, v99
	v_cvt_pk_bf16_f32 v98, v100, v101
	v_cvt_pk_bf16_f32 v99, v102, v103
	global_store_dwordx4 v[236:237], v[96:99], off offset:256
	global_load_dwordx4 v[218:221], v[234:235], off offset:512
	global_load_dwordx4 v[222:225], v[234:235], off offset:528
	s_waitcnt vmcnt(20)
	v_pk_fma_f32 v[90:91], v[90:91], v[42:43], v[228:229]
	v_pk_fma_f32 v[88:89], v[88:89], v[40:41], v[226:227]
	v_pk_fma_f32 v[94:95], v[94:95], v[46:47], v[232:233]
	v_pk_fma_f32 v[92:93], v[92:93], v[44:45], v[230:231]
	v_cvt_pk_bf16_f32 v88, v88, v89
	v_cvt_pk_bf16_f32 v89, v90, v91
	v_cvt_pk_bf16_f32 v90, v92, v93
	v_cvt_pk_bf16_f32 v91, v94, v95
	v_lshl_add_u64 v[236:237], v[236:237], 0, s[96:97]
	global_store_dwordx4 v[236:237], v[88:91], off
	v_lshl_add_u64 v[234:235], v[234:235], 0, s[90:91]
	global_load_dwordx4 v[226:229], v[234:235], off
	global_load_dwordx4 v[230:233], v[234:235], off offset:16
	s_waitcnt vmcnt(21)
	v_pk_fma_f32 v[74:75], v[74:75], v[62:63], v[246:247]
	v_pk_fma_f32 v[72:73], v[72:73], v[60:61], v[244:245]
	v_pk_fma_f32 v[78:79], v[78:79], v[58:59], v[250:251]
	v_pk_fma_f32 v[76:77], v[76:77], v[56:57], v[248:249]
	v_cvt_pk_bf16_f32 v72, v72, v73
	v_cvt_pk_bf16_f32 v73, v74, v75
	v_cvt_pk_bf16_f32 v74, v76, v77
	v_cvt_pk_bf16_f32 v75, v78, v79
	global_store_dwordx4 v[236:237], v[72:75], off offset:256
	global_load_dwordx4 v[244:247], v[234:235], off offset:512
	global_load_dwordx4 v[248:251], v[234:235], off offset:528
	s_waitcnt vmcnt(21)
	v_pk_fma_f32 v[82:83], v[82:83], v[42:43], v[180:181]
	v_pk_fma_f32 v[80:81], v[80:81], v[40:41], v[178:179]
	v_pk_fma_f32 v[86:87], v[86:87], v[46:47], v[184:185]
	v_pk_fma_f32 v[84:85], v[84:85], v[44:45], v[182:183]
	v_cvt_pk_bf16_f32 v80, v80, v81
	v_cvt_pk_bf16_f32 v81, v82, v83
	v_cvt_pk_bf16_f32 v82, v84, v85
	v_cvt_pk_bf16_f32 v83, v86, v87
	v_lshl_add_u64 v[236:237], v[236:237], 0, s[96:97]
	v_lshl_add_u64 v[236:237], v[236:237], 0, s[96:97]
	v_lshl_add_u64 v[236:237], v[236:237], 0, s[96:97]
	v_lshl_add_u64 v[236:237], v[236:237], 0, s[96:97]
	v_lshl_add_u64 v[236:237], v[236:237], 0, s[96:97]
	global_store_dwordx4 v[236:237], v[80:83], off
	s_waitcnt vmcnt(19)
	v_pk_fma_f32 v[66:67], v[66:67], v[62:63], v[188:189]
	v_pk_fma_f32 v[64:65], v[64:65], v[60:61], v[186:187]
	v_pk_fma_f32 v[70:71], v[70:71], v[58:59], v[192:193]
	v_pk_fma_f32 v[68:69], v[68:69], v[56:57], v[190:191]
	v_cvt_pk_bf16_f32 v64, v64, v65
	v_cvt_pk_bf16_f32 v65, v66, v67
	v_cvt_pk_bf16_f32 v66, v68, v69
	v_cvt_pk_bf16_f32 v67, v70, v71
	global_store_dwordx4 v[236:237], v[64:67], off offset:256
	s_waitcnt vmcnt(17)
	v_pk_fma_f32 v[50:51], v[50:51], v[42:43], v[196:197]
	v_pk_fma_f32 v[48:49], v[48:49], v[40:41], v[194:195]
	v_pk_fma_f32 v[54:55], v[54:55], v[46:47], v[200:201]
	v_pk_fma_f32 v[52:53], v[52:53], v[44:45], v[198:199]
	v_cvt_pk_bf16_f32 v48, v48, v49
	v_cvt_pk_bf16_f32 v49, v50, v51
	v_cvt_pk_bf16_f32 v50, v52, v53
	v_cvt_pk_bf16_f32 v51, v54, v55
	v_lshl_add_u64 v[236:237], v[236:237], 0, s[96:97]
	global_store_dwordx4 v[236:237], v[48:51], off
	s_waitcnt vmcnt(15)
	v_pk_fma_f32 v[34:35], v[34:35], v[62:63], v[204:205]
	v_pk_fma_f32 v[32:33], v[32:33], v[60:61], v[202:203]
	v_pk_fma_f32 v[38:39], v[38:39], v[58:59], v[208:209]
	v_pk_fma_f32 v[36:37], v[36:37], v[56:57], v[206:207]
	v_cvt_pk_bf16_f32 v32, v32, v33
	v_cvt_pk_bf16_f32 v33, v34, v35
	v_cvt_pk_bf16_f32 v34, v36, v37
	v_cvt_pk_bf16_f32 v35, v38, v39
	global_store_dwordx4 v[236:237], v[32:35], off offset:256
	s_waitcnt vmcnt(13)
	v_pk_fma_f32 v[26:27], v[26:27], v[42:43], v[212:213]
	v_pk_fma_f32 v[24:25], v[24:25], v[40:41], v[210:211]
	v_pk_fma_f32 v[30:31], v[30:31], v[46:47], v[216:217]
	v_pk_fma_f32 v[28:29], v[28:29], v[44:45], v[214:215]
	v_cvt_pk_bf16_f32 v24, v24, v25
	v_cvt_pk_bf16_f32 v25, v26, v27
	v_cvt_pk_bf16_f32 v26, v28, v29
	v_cvt_pk_bf16_f32 v27, v30, v31
	v_lshl_add_u64 v[236:237], v[236:237], 0, s[96:97]
	global_store_dwordx4 v[236:237], v[24:27], off
	s_waitcnt vmcnt(11)
	v_pk_fma_f32 v[18:19], v[18:19], v[62:63], v[220:221]
	v_pk_fma_f32 v[16:17], v[16:17], v[60:61], v[218:219]
	v_pk_fma_f32 v[22:23], v[22:23], v[58:59], v[224:225]
	v_pk_fma_f32 v[20:21], v[20:21], v[56:57], v[222:223]
	v_cvt_pk_bf16_f32 v16, v16, v17
	v_cvt_pk_bf16_f32 v17, v18, v19
	v_cvt_pk_bf16_f32 v18, v20, v21
	v_cvt_pk_bf16_f32 v19, v22, v23
	global_store_dwordx4 v[236:237], v[16:19], off offset:256
	s_waitcnt vmcnt(9)
	v_pk_fma_f32 v[6:7], v[6:7], v[42:43], v[228:229]
	v_pk_fma_f32 v[4:5], v[4:5], v[40:41], v[226:227]
	v_pk_fma_f32 v[10:11], v[10:11], v[46:47], v[232:233]
	v_pk_fma_f32 v[8:9], v[8:9], v[44:45], v[230:231]
	v_cvt_pk_bf16_f32 v4, v4, v5
	v_cvt_pk_bf16_f32 v5, v6, v7
	v_cvt_pk_bf16_f32 v6, v8, v9
	v_cvt_pk_bf16_f32 v7, v10, v11
	v_lshl_add_u64 v[236:237], v[236:237], 0, s[96:97]
	global_store_dwordx4 v[236:237], v[4:7], off
	s_waitcnt vmcnt(7)
	v_pk_fma_f32 v[14:15], v[14:15], v[62:63], v[246:247]
	v_pk_fma_f32 v[12:13], v[12:13], v[60:61], v[244:245]
	v_pk_fma_f32 v[2:3], v[2:3], v[58:59], v[250:251]
	v_pk_fma_f32 v[0:1], v[0:1], v[56:57], v[248:249]
	v_cvt_pk_bf16_f32 v12, v12, v13
	v_cvt_pk_bf16_f32 v13, v14, v15
	v_cvt_pk_bf16_f32 v14, v0, v1
	v_cvt_pk_bf16_f32 v15, v2, v3
	global_store_dwordx4 v[236:237], v[12:15], off offset:256
	s_cbranch_vccnz .LBB0_491
	s_andn2_b64 vcc, exec, s[12:13]
	s_cbranch_vccnz .LBB0_490
	s_barrier
	s_branch .LBB0_490

	.amdhsa_kernel _Z3fwdILj131071EEv4Args
		.amdhsa_group_segment_fixed_size 0
		.amdhsa_private_segment_fixed_size 0
		.amdhsa_kernarg_size 584
		.amdhsa_user_sgpr_count 2
		.amdhsa_user_sgpr_dispatch_ptr 0
		.amdhsa_user_sgpr_queue_ptr 0
		.amdhsa_user_sgpr_kernarg_segment_ptr 1
		.amdhsa_user_sgpr_dispatch_id 0
		.amdhsa_user_sgpr_kernarg_preload_length 0
		.amdhsa_user_sgpr_kernarg_preload_offset 0
		.amdhsa_user_sgpr_private_segment_size 0
		.amdhsa_uses_dynamic_stack 0
		.amdhsa_enable_private_segment 0
		.amdhsa_system_sgpr_workgroup_id_x 1
		.amdhsa_system_sgpr_workgroup_id_y 0
		.amdhsa_system_sgpr_workgroup_id_z 0
		.amdhsa_system_sgpr_workgroup_info 0
		.amdhsa_system_vgpr_workitem_id 0
		.amdhsa_next_free_vgpr 256
		.amdhsa_next_free_sgpr 98
		.amdhsa_accum_offset 256
		.amdhsa_reserve_vcc 1
		.amdhsa_float_round_mode_32 0
		.amdhsa_float_round_mode_16_64 0
		.amdhsa_float_denorm_mode_32 3
		.amdhsa_float_denorm_mode_16_64 3
		.amdhsa_dx10_clamp 1
		.amdhsa_ieee_mode 1
		.amdhsa_fp16_overflow 0
		.amdhsa_tg_split 0
		.amdhsa_exception_fp_ieee_invalid_op 0
		.amdhsa_exception_fp_denorm_src 0
		.amdhsa_exception_fp_ieee_div_zero 0
		.amdhsa_exception_fp_ieee_overflow 0
		.amdhsa_exception_fp_ieee_underflow 0
		.amdhsa_exception_fp_ieee_inexact 0
		.amdhsa_exception_int_div_zero 0
	.end_amdhsa_kernel

amdhsa.kernels:
  - .agpr_count:     0
    .args:
      - .offset:         0
        .size:           328
        .value_kind:     by_value
      - .offset:         328
        .size:           4
        .value_kind:     hidden_block_count_x
      - .offset:         332
        .size:           4
        .value_kind:     hidden_block_count_y
      - .offset:         336
        .size:           4
        .value_kind:     hidden_block_count_z
      - .offset:         340
        .size:           2
        .value_kind:     hidden_group_size_x
      - .offset:         342
        .size:           2
        .value_kind:     hidden_group_size_y
      - .offset:         344
        .size:           2
        .value_kind:     hidden_group_size_z
      - .offset:         346
        .size:           2
        .value_kind:     hidden_remainder_x
      - .offset:         348
        .size:           2
        .value_kind:     hidden_remainder_y
      - .offset:         350
        .size:           2
        .value_kind:     hidden_remainder_z
      - .offset:         368
        .size:           8
        .value_kind:     hidden_global_offset_x
      - .offset:         376
        .size:           8
        .value_kind:     hidden_global_offset_y
      - .offset:         384
        .size:           8
        .value_kind:     hidden_global_offset_z
      - .offset:         392
        .size:           2
        .value_kind:     hidden_grid_dims
      - .offset:         448
        .size:           4
        .value_kind:     hidden_dynamic_lds_size
    .group_segment_fixed_size: 0
    .kernarg_segment_align: 8
    .kernarg_segment_size: 584
    .language:       OpenCL C
    .language_version:
      - 2
      - 0
    .max_flat_workgroup_size: 512
    .name:           _Z3fwdILj131071EEv4Args
    .private_segment_fixed_size: 0
    .sgpr_count:     104
    .sgpr_spill_count: 721
    .symbol:         _Z3fwdILj131071EEv4Args.kd
    .uniform_work_group_size: 1
    .uses_dynamic_stack: false
    .vgpr_count:     256
    .vgpr_spill_count: 0
    .wavefront_size: 64
